# combine loop, layer-0 fused norm sections: second column half's 6 table loads requested with the first half's (registers dead there), one table round trip per token instead of two
# speedup vs baseline: 1.0054x; 1.0054x over previous
; DEV unsigned cvtpk(float lo, float hi) { f32x2 v = {lo, hi}; bf16v2 r = __builtin_convertvector(v, bf16v2); return __builtin_bit_cast(unsigned, r); }
; DEV unsigned cvtpk_h(float lo, float hi) { f32x2 v = {lo, hi}; f16x2 r = __builtin_convertvector(v, f16x2); return __builtin_bit_cast(unsigned, r); }
; DEV unsigned pk_fp8x4(float a, float b, float c, float d) { int w = __builtin_amdgcn_cvt_pk_fp8_f32(a, b, 0, false); w = __builtin_amdgcn_cvt_pk_fp8_f32(c, d, w, true); return (unsigned)w; }
; DEV float fast_rsq(float x) { return __builtin_amdgcn_rsqf(x); }
; DEV float wave_sum(float v) { v = half_sum(v); v += lx16(v); v += lr8(v); v += lr4(v); v += lx2(v); v += lx1(v); return v; }
; DEV void norm_store(const Params& p, int tok, const float (&xv)[2][8], const float* __restrict__ gain, const float* __restrict__ sh, const float* __restrict__ scl, bool with_lo, int lane) {
;     ...
;     ss = wave_sum(ss);
;     const float rinv = fast_rsq(ss * (1.0f / 1024.0f) + EPS);
;     bf16_t* H = (bf16_t*)(p.ws + WS_H) + (size_t)tok * HLD;
; #pragma unroll
;     for (int j = 0; j < 2; ++j) { const int col = 8 * lane + 512 * j; float y[8];
;         const f32x4 g0 = *(const f32x4*)(gain + col), g1 = *(const f32x4*)(gain + col + 4), s0 = *(const f32x4*)(scl + col), s1 = *(const f32x4*)(scl + col + 4), h0 = *(const f32x4*)(sh + col), h1 = *(const f32x4*)(sh + col + 4);
; #pragma unroll
;         for (int i = 0; i < 4; ++i) { y[i] = xv[j][i] * rinv * g0[i] * (1.0f + s0[i]) + h0[i]; y[4 + i] = xv[j][4 + i] * rinv * g1[i] * (1.0f + s1[i]) + h1[i]; }
;         if (!with_lo) { const u32x4 w = {cvtpk(y[0], y[1]), cvtpk(y[2], y[3]), cvtpk(y[4], y[5]), cvtpk(y[6], y[7])}; *(u32x4*)(H + col) = w; }
;         else { *(u32x2*)((unsigned char*)H + col) = (u32x2){pk_fp8x4(y[0], y[1], y[2], y[3]), pk_fp8x4(y[4], y[5], y[6], y[7])};
;             const u32x4 wl = {cvtpk_h(y[0], y[1]), cvtpk_h(y[2], y[3]), cvtpk_h(y[4], y[5]), cvtpk_h(y[6], y[7])};
;             *(u32x4*)(H + 1024 + col) = wl; } }
; DEV void phase_combine(const Params& p, int layer, LAS char* lds, bool have_tables = false) {
;     ...
;             if (layer == 0) { const float* m = modn + mod_row(tok) * 6144; norm_store(p, tok, xv, p.norm_mix + 1024, m, m + 1024, false, lane); } }
.LBB0_1501:
	v_readlane_b32 s2, v254, 36
	v_readlane_b32 s3, v254, 37
	s_andn2_b64 vcc, exec, s[2:3]
	v_lshl_add_u64 v[88:89], v[128:129], 0, v[126:127]
	v_cndmask_b32_e64 v82, 0, 1, s[2:3]
	v_cmp_ne_u32_e64 s[42:43], 1, v82
	s_cbranch_vccnz .LBB0_1503
	v_pk_mul_f32 v[82:83], v[96:97], v[96:97]
	v_pk_mul_f32 v[110:111], v[98:99], v[98:99]
	v_add_f32_e32 v82, v82, v83
	v_add_f32_e32 v82, v110, v82
	v_lshl_add_u64 v[90:91], v[112:113], 2, s[48:49]
	v_pk_mul_f32 v[112:113], v[100:101], v[100:101]
	v_add_f32_e32 v82, v111, v82
	v_add_f32_e32 v82, v112, v82
	v_pk_mul_f32 v[114:115], v[102:103], v[102:103]
	v_add_f32_e32 v82, v113, v82
	v_add_f32_e32 v82, v114, v82
	v_pk_mul_f32 v[144:145], v[92:93], v[92:93]
	v_add_f32_e32 v82, v115, v82
	v_add_f32_e32 v82, v82, v144
	v_pk_mul_f32 v[146:147], v[94:95], v[94:95]
	v_add_f32_e32 v82, v145, v82
	v_add_f32_e32 v82, v146, v82
	v_pk_mul_f32 v[148:149], v[84:85], v[84:85]
	v_add_f32_e32 v82, v147, v82
	v_add_f32_e32 v82, v148, v82
	v_pk_mul_f32 v[150:151], v[86:87], v[86:87]
	v_add_f32_e32 v82, v149, v82
	s_mov_b64 s[2:3], 0x1000
	v_add_f32_e32 v82, v150, v82
	v_lshl_add_u64 v[108:109], v[90:91], 0, s[2:3]
	v_add_f32_e32 v82, v151, v82
	v_mov_b32_e32 v83, v82
	v_lshl_add_u64 v[114:115], v[108:109], 0, v[178:179]
	s_nop 1
	v_permlane32_swap_b32 v82, v83
	s_nop 1
	global_load_dwordx4 v[110:113], v[118:119], off offset:16
	global_load_dwordx4 v[144:147], v[118:119], off
	global_load_dwordx4 v[148:151], v[114:115], off offset:16
	global_load_dwordx4 v[152:155], v[114:115], off
	v_lshl_add_u64 v[90:91], v[90:91], 0, v[178:179]
	global_load_dwordx4 v[156:159], v[90:91], off offset:16
	global_load_dwordx4 v[160:163], v[90:91], off
	v_lshl_add_u64 v[184:185], v[108:109], 0, v[188:189]
	global_load_dwordx4 v[166:169], v[120:121], off offset:16
	global_load_dwordx4 v[170:173], v[120:121], off
	global_load_dwordx4 v[174:177], v[184:185], off offset:16
	global_load_dwordx4 v[198:201], v[184:185], off
	global_load_dwordx4 v[222:225], v[90:91], off offset:2064
	global_load_dwordx4 v[232:235], v[90:91], off offset:2048
	v_add_f32_e32 v82, v82, v83
	ds_swizzle_b32 v83, v82 offset:swizzle(SWAP,16)
	v_mov_b32_e32 v105, v179
	s_waitcnt lgkmcnt(0)
	v_add_f32_e32 v82, v82, v83
	s_nop 1
	v_add_f32_dpp v82, v82, v82 row_ror:8 row_mask:0xf bank_mask:0xf bound_ctrl:1
	s_waitcnt vmcnt(8)
	v_pk_add_f32 v[114:115], v[152:153], 1.0 op_sel_hi:[1,0]
	v_add_f32_dpp v82, v82, v82 row_ror:4 row_mask:0xf bank_mask:0xf bound_ctrl:1
	v_add_co_u32_e32 v152, vcc, s35, v88
	s_nop 0
	v_add_f32_dpp v82, v82, v82 quad_perm:[2,3,0,1] row_mask:0xf bank_mask:0xf bound_ctrl:1
	v_addc_co_u32_e32 v153, vcc, 0, v89, vcc
	s_nop 0
	v_add_f32_dpp v82, v82, v82 quad_perm:[1,0,3,2] row_mask:0xf bank_mask:0xf bound_ctrl:1
	v_fmamk_f32 v82, v82, 0x3a800000, v0
	v_rsq_f32_e32 v82, v82
	s_nop 0
	v_pk_mul_f32 v[100:101], v[100:101], v[82:83] op_sel_hi:[1,0]
	s_nop 0
	v_pk_mul_f32 v[100:101], v[110:111], v[100:101]
	v_pk_add_f32 v[110:111], v[148:149], 1.0 op_sel_hi:[1,0]
	v_pk_mul_f32 v[98:99], v[98:99], v[82:83] op_sel_hi:[1,0]
	v_pk_mul_f32 v[96:97], v[96:97], v[82:83] op_sel_hi:[1,0]
	s_waitcnt vmcnt(7)
	v_pk_fma_f32 v[100:101], v[110:111], v[100:101], v[156:157]
	v_pk_mul_f32 v[98:99], v[146:147], v[98:99]
	v_pk_add_f32 v[110:111], v[154:155], 1.0 op_sel_hi:[1,0]
	v_pk_mul_f32 v[102:103], v[102:103], v[82:83] op_sel_hi:[1,0]
	v_pk_mul_f32 v[96:97], v[144:145], v[96:97]
	s_waitcnt vmcnt(6)
	v_pk_fma_f32 v[98:99], v[110:111], v[98:99], v[162:163]
	v_pk_mul_f32 v[102:103], v[112:113], v[102:103]
	v_pk_add_f32 v[110:111], v[150:151], 1.0 op_sel_hi:[1,0]
	v_pk_fma_f32 v[96:97], v[114:115], v[96:97], v[160:161]
	v_pk_fma_f32 v[102:103], v[110:111], v[102:103], v[158:159]
	v_cvt_pk_bf16_f32 v96, v96, v97
	v_cvt_pk_bf16_f32 v97, v98, v99
	v_cvt_pk_bf16_f32 v98, v100, v101
	v_cvt_pk_bf16_f32 v99, v102, v103
	global_store_dwordx4 v[152:153], v[96:99], off offset:256
	s_nop 0
	v_lshl_add_u64 v[112:113], v[108:109], 0, v[104:105]
	s_nop 0
	s_nop 0
	v_pk_mul_f32 v[90:91], v[92:93], v[82:83] op_sel_hi:[1,0]
	v_pk_mul_f32 v[84:85], v[84:85], v[82:83] op_sel_hi:[1,0]
	s_waitcnt vmcnt(1)
	v_pk_add_f32 v[92:93], v[198:199], 1.0 op_sel_hi:[1,0]
	v_pk_mul_f32 v[90:91], v[90:91], v[170:171]
	v_pk_mul_f32 v[84:85], v[84:85], v[166:167]
	s_waitcnt vmcnt(1)
	v_pk_fma_f32 v[90:91], v[90:91], v[92:93], v[232:233]
	v_pk_add_f32 v[92:93], v[174:175], 1.0 op_sel_hi:[1,0]
	s_nop 0
	v_pk_fma_f32 v[84:85], v[84:85], v[92:93], v[222:223]
	v_pk_mul_f32 v[92:93], v[94:95], v[82:83] op_sel_hi:[1,0]
	v_pk_mul_f32 v[82:83], v[86:87], v[82:83] op_sel_hi:[1,0]
	v_pk_mul_f32 v[92:93], v[92:93], v[172:173]
	v_pk_add_f32 v[94:95], v[200:201], 1.0 op_sel_hi:[1,0]
	v_pk_mul_f32 v[82:83], v[82:83], v[168:169]
	v_pk_add_f32 v[86:87], v[176:177], 1.0 op_sel_hi:[1,0]
	v_pk_fma_f32 v[92:93], v[92:93], v[94:95], v[234:235]
	v_pk_fma_f32 v[86:87], v[82:83], v[86:87], v[224:225]
	v_cvt_pk_bf16_f32 v82, v90, v91
	v_cvt_pk_bf16_f32 v83, v92, v93
	v_cvt_pk_bf16_f32 v84, v84, v85
	v_cvt_pk_bf16_f32 v85, v86, v87
	global_store_dwordx4 v[152:153], v[82:85], off offset:1280

; DEV unsigned cvtpk(float lo, float hi) { f32x2 v = {lo, hi}; bf16v2 r = __builtin_convertvector(v, bf16v2); return __builtin_bit_cast(unsigned, r); }
; DEV unsigned cvtpk_h(float lo, float hi) { f32x2 v = {lo, hi}; f16x2 r = __builtin_convertvector(v, f16x2); return __builtin_bit_cast(unsigned, r); }
; DEV unsigned pk_fp8x4(float a, float b, float c, float d) { int w = __builtin_amdgcn_cvt_pk_fp8_f32(a, b, 0, false); w = __builtin_amdgcn_cvt_pk_fp8_f32(c, d, w, true); return (unsigned)w; }
; DEV float fast_rsq(float x) { return __builtin_amdgcn_rsqf(x); }
; DEV float wave_sum(float v) { v = half_sum(v); v += lx16(v); v += lr8(v); v += lr4(v); v += lx2(v); v += lx1(v); return v; }
; DEV void norm_store(const Params& p, int tok, const float (&xv)[2][8], const float* __restrict__ gain, const float* __restrict__ sh, const float* __restrict__ scl, bool with_lo, int lane) {
;     ...
;     ss = wave_sum(ss);
;     const float rinv = fast_rsq(ss * (1.0f / 1024.0f) + EPS);
;     bf16_t* H = (bf16_t*)(p.ws + WS_H) + (size_t)tok * HLD;
; #pragma unroll
;     for (int j = 0; j < 2; ++j) { const int col = 8 * lane + 512 * j; float y[8];
;         const f32x4 g0 = *(const f32x4*)(gain + col), g1 = *(const f32x4*)(gain + col + 4), s0 = *(const f32x4*)(scl + col), s1 = *(const f32x4*)(scl + col + 4), h0 = *(const f32x4*)(sh + col), h1 = *(const f32x4*)(sh + col + 4);
; #pragma unroll
;         for (int i = 0; i < 4; ++i) { y[i] = xv[j][i] * rinv * g0[i] * (1.0f + s0[i]) + h0[i]; y[4 + i] = xv[j][4 + i] * rinv * g1[i] * (1.0f + s1[i]) + h1[i]; }
;         if (!with_lo) { const u32x4 w = {cvtpk(y[0], y[1]), cvtpk(y[2], y[3]), cvtpk(y[4], y[5]), cvtpk(y[6], y[7])}; *(u32x4*)(H + col) = w; }
;         else { *(u32x2*)((unsigned char*)H + col) = (u32x2){pk_fp8x4(y[0], y[1], y[2], y[3]), pk_fp8x4(y[4], y[5], y[6], y[7])};
;             const u32x4 wl = {cvtpk_h(y[0], y[1]), cvtpk_h(y[2], y[3]), cvtpk_h(y[4], y[5]), cvtpk_h(y[6], y[7])};
;             *(u32x4*)(H + 1024 + col) = wl; } }
; DEV void phase_combine(const Params& p, int layer, LAS char* lds, bool have_tables = false) {
;     ...
;             if (layer == 0) { const float* m = modn + mod_row(tok) * 6144; norm_store(p, tok, xv, p.norm_mix + 1024, m, m + 1024, false, lane); } }
.LBB0_1512:
	v_pk_mul_f32 v[66:67], v[82:83], v[82:83]
	v_pk_mul_f32 v[68:69], v[84:85], v[84:85]
	v_add_f32_e32 v66, v66, v67
	v_add_f32_e32 v66, v68, v66
	v_pk_mul_f32 v[74:75], v[70:71], v[70:71]
	v_add_f32_e32 v66, v69, v66
	v_add_f32_e32 v66, v74, v66
	v_pk_mul_f32 v[76:77], v[72:73], v[72:73]
	v_add_f32_e32 v66, v75, v66
	v_add_f32_e32 v66, v76, v66
	v_pk_mul_f32 v[78:79], v[62:63], v[62:63]
	v_add_f32_e32 v66, v77, v66
	v_add_f32_e32 v66, v66, v78
	v_pk_mul_f32 v[80:81], v[64:65], v[64:65]
	v_add_f32_e32 v66, v79, v66
	v_add_f32_e32 v66, v80, v66
	v_pk_mul_f32 v[90:91], v[58:59], v[58:59]
	v_add_f32_e32 v66, v81, v66
	v_add_f32_e32 v66, v90, v66
	v_pk_mul_f32 v[92:93], v[60:61], v[60:61]
	v_add_f32_e32 v66, v91, v66
	v_lshl_add_u64 v[86:87], v[86:87], 2, s[48:49]
	s_mov_b64 s[2:3], 0x1000
	v_add_f32_e32 v66, v92, v66
	v_lshl_add_u64 v[102:103], v[86:87], 0, s[2:3]
	v_add_f32_e32 v105, v93, v66
	v_mov_b32_e32 v106, v105
	v_lshl_add_u64 v[90:91], v[102:103], 0, v[178:179]
	s_nop 1
	v_permlane32_swap_b32 v106, v105
	s_nop 1
	global_load_dwordx4 v[66:69], v[118:119], off
	global_load_dwordx4 v[74:77], v[90:91], off
	global_load_dwordx4 v[78:81], v[118:119], off offset:16
	s_nop 0
	global_load_dwordx4 v[90:93], v[90:91], off offset:16
	v_lshl_add_u64 v[86:87], v[86:87], 0, v[178:179]
	global_load_dwordx4 v[94:97], v[86:87], off
	global_load_dwordx4 v[98:101], v[86:87], off offset:16
	v_lshl_add_u64 v[184:185], v[102:103], 0, v[188:189]
	global_load_dwordx4 v[202:205], v[120:121], off
	global_load_dwordx4 v[210:213], v[184:185], off
	global_load_dwordx4 v[214:217], v[120:121], off offset:16
	global_load_dwordx4 v[228:231], v[184:185], off offset:16
	global_load_dwordx4 v[238:241], v[86:87], off offset:2048
	global_load_dwordx4 v[242:245], v[86:87], off offset:2064
	v_add_f32_e32 v105, v106, v105
	ds_swizzle_b32 v106, v105 offset:swizzle(SWAP,16)
	s_mov_b32 s2, 0x21711000
	v_add_co_u32_e32 v108, vcc, s2, v88
	s_waitcnt lgkmcnt(0)
	v_add_f32_e32 v105, v105, v106
	v_addc_co_u32_e32 v109, vcc, 0, v89, vcc
	s_nop 0
	v_add_f32_dpp v105, v105, v105 row_ror:8 row_mask:0xf bank_mask:0xf bound_ctrl:1
	s_waitcnt vmcnt(10)
	v_pk_add_f32 v[74:75], v[74:75], 1.0 op_sel_hi:[1,0]
	v_add_f32_dpp v105, v105, v105 row_ror:4 row_mask:0xf bank_mask:0xf bound_ctrl:1
	v_pk_add_f32 v[76:77], v[76:77], 1.0 op_sel_hi:[1,0]
	s_nop 0
	v_add_f32_dpp v105, v105, v105 quad_perm:[2,3,0,1] row_mask:0xf bank_mask:0xf bound_ctrl:1
	s_nop 1
	v_add_f32_dpp v105, v105, v105 quad_perm:[1,0,3,2] row_mask:0xf bank_mask:0xf bound_ctrl:1
	v_fmamk_f32 v105, v105, 0x3a800000, v0
	v_rsq_f32_e32 v106, v105
	v_mov_b32_e32 v105, v179
	v_lshl_add_u64 v[88:89], v[102:103], 0, v[104:105]
	v_pk_mul_f32 v[82:83], v[82:83], v[106:107] op_sel_hi:[1,0]
	v_pk_mul_f32 v[70:71], v[70:71], v[106:107] op_sel_hi:[1,0]
	v_pk_mul_f32 v[84:85], v[84:85], v[106:107] op_sel_hi:[1,0]
	v_pk_mul_f32 v[72:73], v[72:73], v[106:107] op_sel_hi:[1,0]
	v_pk_mul_f32 v[66:67], v[66:67], v[82:83]
	s_waitcnt vmcnt(9)
	v_pk_mul_f32 v[70:71], v[78:79], v[70:71]
	s_waitcnt vmcnt(8)
	v_pk_add_f32 v[78:79], v[90:91], 1.0 op_sel_hi:[1,0]
	v_pk_mul_f32 v[68:69], v[68:69], v[84:85]
	v_pk_mul_f32 v[72:73], v[80:81], v[72:73]
	v_pk_add_f32 v[80:81], v[92:93], 1.0 op_sel_hi:[1,0]
	s_waitcnt vmcnt(7)
	v_pk_fma_f32 v[66:67], v[74:75], v[66:67], v[94:95]
	s_waitcnt vmcnt(6)
	v_pk_fma_f32 v[70:71], v[78:79], v[70:71], v[98:99]
	v_pk_fma_f32 v[68:69], v[76:77], v[68:69], v[96:97]
	v_pk_fma_f32 v[72:73], v[80:81], v[72:73], v[100:101]
	v_cvt_pk_bf16_f32 v66, v66, v67
	v_cvt_pk_bf16_f32 v67, v68, v69
	v_cvt_pk_bf16_f32 v68, v70, v71
	v_cvt_pk_bf16_f32 v69, v72, v73
	global_store_dwordx4 v[108:109], v[66:69], off offset:384
	s_nop 0
	s_nop 0
	v_pk_mul_f32 v[62:63], v[62:63], v[106:107] op_sel_hi:[1,0]
	v_pk_mul_f32 v[58:59], v[58:59], v[106:107] op_sel_hi:[1,0]
	v_pk_mul_f32 v[64:65], v[64:65], v[106:107] op_sel_hi:[1,0]
	v_pk_mul_f32 v[60:61], v[60:61], v[106:107] op_sel_hi:[1,0]
	s_waitcnt vmcnt(1)
	v_pk_mul_f32 v[62:63], v[62:63], v[202:203]
	s_waitcnt vmcnt(1)
	v_pk_add_f32 v[66:67], v[210:211], 1.0 op_sel_hi:[1,0]
	s_waitcnt vmcnt(1)
	v_pk_mul_f32 v[58:59], v[58:59], v[214:215]
	s_waitcnt vmcnt(1)
	v_pk_add_f32 v[70:71], v[228:229], 1.0 op_sel_hi:[1,0]
	v_pk_mul_f32 v[64:65], v[64:65], v[204:205]
	v_pk_add_f32 v[68:69], v[212:213], 1.0 op_sel_hi:[1,0]
	v_pk_mul_f32 v[60:61], v[60:61], v[216:217]
	v_pk_add_f32 v[72:73], v[230:231], 1.0 op_sel_hi:[1,0]
	s_waitcnt vmcnt(1)
	v_pk_fma_f32 v[62:63], v[62:63], v[66:67], v[238:239]
	s_waitcnt vmcnt(1)
	v_pk_fma_f32 v[66:67], v[58:59], v[70:71], v[242:243]
	v_pk_fma_f32 v[64:65], v[64:65], v[68:69], v[240:241]
	v_pk_fma_f32 v[68:69], v[60:61], v[72:73], v[244:245]
	v_cvt_pk_bf16_f32 v58, v62, v63
	v_cvt_pk_bf16_f32 v59, v64, v65
	v_cvt_pk_bf16_f32 v60, v66, v67
	v_cvt_pk_bf16_f32 v61, v68, v69
	global_store_dwordx4 v[108:109], v[58:61], off offset:1408
	s_branch .LBB0_1486
